# plus MoE-up gather offsets batched (4 loads one wait) and w_out epilogue: gate vectors loaded once, counted vmcnt(8) keeps residual prefetch in flight
# speedup vs baseline: 1.0115x; 1.0115x over previous
;     __device__ __forceinline__ void load(Regs& r, const pg::Unit& u, int g, int wr, int wc, int fr, int fq) const {
;         EPI_G(g)
; #pragma unroll
;         for (int bj = 0; bj < 2; ++bj)
; #pragma unroll
;             for (int n = 0; n < 2; ++n) r.x[bj][n] = *(const f32x4*)(xin + (size_t)row * DM + u.pn * 256 + bj * 128 + wc * 32 + 16 * n + 4 * fq);
;     }
;     __device__ __forceinline__ void finish(const Regs& r, const pg::Acc& acc, const pg::Unit& u, int g, int wr, int wc, int fr, int fq) const {
;         EPI_G(g)
;         const int b = (u.pm * 256) / SEQ;
; #pragma unroll
;         for (int bj = 0; bj < 2; ++bj)
; #pragma unroll
;             for (int n = 0; n < 2; ++n) { const int col = u.pn * 256 + bj * 128 + wc * 32 + 16 * n + 4 * fq;
;                 const f32x4 gv = *(const f32x4*)(gacc + (size_t)b * (NMOD * DM) + col);
;                 *(f32x4*)(xout + (size_t)row * DM + col) = r.x[bj][n] + gv * (acc[ai][bj][m][n] * isc); }
;     }
.LBB0_1277:
	s_lshl_b32 s24, s33, 8
	v_add_u32_e32 v2, s24, v1
	v_ashrrev_i32_e32 v3, 31, v2
	s_lshl_b32 s22, s20, 8
	v_lshlrev_b64 v[54:55], 13, v[2:3]
	s_ashr_i32 s23, s22, 31
	v_lshl_add_u64 v[2:3], s[0:1], 0, v[54:55]
	s_lshl_b64 s[20:21], s[22:23], 2
	v_lshl_add_u64 v[2:3], v[2:3], 0, s[20:21]
	s_mov_b32 s13, s7
	v_lshl_add_u64 v[2:3], v[2:3], 0, s[12:13]
	v_mov_b32_e32 v207, v199
	v_lshl_add_u64 v[2:3], v[2:3], 0, v[206:207]
	s_or_b32 s17, s24, 16
	global_load_dwordx4 v[6:9], v[2:3], off
	global_load_dwordx4 v[10:13], v[2:3], off offset:64
	global_load_dwordx4 v[14:17], v[2:3], off offset:512
	global_load_dwordx4 v[18:21], v[2:3], off offset:576
	v_add_u32_e32 v2, s17, v1
	v_ashrrev_i32_e32 v3, 31, v2
	v_lshlrev_b64 v[56:57], 13, v[2:3]
	v_lshl_add_u64 v[2:3], s[0:1], 0, v[56:57]
	s_ashr_i32 s23, s33, 31
	v_lshl_add_u64 v[2:3], v[2:3], 0, s[20:21]
	s_lshr_b32 s23, s23, 28
	v_lshl_add_u64 v[2:3], v[2:3], 0, s[12:13]
	s_add_i32 s23, s33, s23
	v_lshl_add_u64 v[2:3], v[2:3], 0, v[206:207]
	s_ashr_i32 s23, s23, 4
	global_load_dwordx4 v[22:25], v[2:3], off
	global_load_dwordx4 v[26:29], v[2:3], off offset:64
	global_load_dwordx4 v[30:33], v[2:3], off offset:512
	global_load_dwordx4 v[34:37], v[2:3], off offset:576
	s_mul_hi_i32 s25, s23, 0xc000
	s_mul_i32 s23, s23, 0xc000
	v_or_b32_e32 v2, s22, v221
	s_add_u32 s22, s44, s23
	v_ashrrev_i32_e32 v3, 31, v2
	s_addc_u32 s23, s45, s25
	v_lshlrev_b64 v[2:3], 2, v[2:3]
	v_lshl_add_u64 v[4:5], s[22:23], 0, v[2:3]
	global_load_dwordx4 v[38:41], v[4:5], off
	global_load_dwordx4 v[42:45], v[4:5], off offset:64
	global_load_dwordx4 v[46:49], v[4:5], off offset:512
	global_load_dwordx4 v[50:53], v[4:5], off offset:576
	s_or_b32 s22, s24, 32
	v_pk_mul_f32 v[58:59], v[180:181], s[14:15] op_sel_hi:[1,0]
	v_pk_mul_f32 v[180:181], v[186:187], s[14:15] op_sel_hi:[1,0]
	v_add_u32_e32 v186, s22, v1
	v_ashrrev_i32_e32 v187, 31, v186
	v_lshlrev_b64 v[186:187], 13, v[186:187]
	v_pk_mul_f32 v[60:61], v[178:179], s[14:15] op_sel_hi:[1,0]
	v_pk_mul_f32 v[178:179], v[188:189], s[14:15] op_sel_hi:[1,0]
	v_lshl_add_u64 v[54:55], s[8:9], 0, v[54:55]
	v_lshl_add_u64 v[188:189], s[0:1], 0, v[186:187]
	v_pk_mul_f32 v[62:63], v[184:185], s[14:15] op_sel_hi:[1,0]
	v_pk_mul_f32 v[64:65], v[182:183], s[14:15] op_sel_hi:[1,0]
	v_pk_mul_f32 v[182:183], v[192:193], s[14:15] op_sel_hi:[1,0]
	v_pk_mul_f32 v[184:185], v[190:191], s[14:15] op_sel_hi:[1,0]
	v_lshl_add_u64 v[54:55], v[54:55], 0, v[2:3]
	v_lshl_add_u64 v[188:189], v[188:189], 0, s[20:21]
	v_lshl_add_u64 v[188:189], v[188:189], 0, s[12:13]
	v_lshl_add_u64 v[188:189], v[188:189], 0, v[206:207]
	s_or_b32 s23, s24, 48
	v_lshl_add_u64 v[56:57], s[8:9], 0, v[56:57]
	v_lshl_add_u64 v[56:57], v[56:57], 0, v[2:3]
	s_andn2_b64 vcc, exec, s[2:3]
	s_mov_b64 s[2:3], -1
	s_waitcnt vmcnt(0)
	v_pk_fma_f32 v[8:9], v[58:59], v[40:41], v[8:9]
	v_pk_fma_f32 v[6:7], v[60:61], v[38:39], v[6:7]
	v_pk_fma_f32 v[12:13], v[62:63], v[44:45], v[12:13]
	v_pk_fma_f32 v[10:11], v[64:65], v[42:43], v[10:11]
	v_pk_fma_f32 v[16:17], v[178:179], v[48:49], v[16:17]
	v_pk_fma_f32 v[14:15], v[180:181], v[46:47], v[14:15]
	v_pk_fma_f32 v[20:21], v[182:183], v[52:53], v[20:21]
	v_pk_fma_f32 v[18:19], v[184:185], v[50:51], v[18:19]
	global_store_dwordx4 v[54:55], v[6:9], off
	global_store_dwordx4 v[54:55], v[10:13], off offset:64
	global_store_dwordx4 v[54:55], v[14:17], off offset:512
	global_store_dwordx4 v[54:55], v[18:21], off offset:576
	global_load_dwordx4 v[6:9], v[188:189], off offset:576
	global_load_dwordx4 v[10:13], v[188:189], off offset:512
	global_load_dwordx4 v[14:17], v[188:189], off offset:64
	global_load_dwordx4 v[18:21], v[188:189], off
	v_pk_mul_f32 v[60:61], v[168:169], s[14:15] op_sel_hi:[1,0]
	v_add_u32_e32 v168, s23, v1
	v_ashrrev_i32_e32 v169, 31, v168
	v_lshlrev_b64 v[168:169], 13, v[168:169]
	v_pk_mul_f32 v[54:55], v[164:165], s[14:15] op_sel_hi:[1,0]
	v_pk_mul_f32 v[58:59], v[162:163], s[14:15] op_sel_hi:[1,0]
	v_pk_mul_f32 v[162:163], v[170:171], s[14:15] op_sel_hi:[1,0]
	v_lshl_add_u64 v[170:171], s[0:1], 0, v[168:169]
	v_pk_mul_f32 v[62:63], v[166:167], s[14:15] op_sel_hi:[1,0]
	v_pk_mul_f32 v[64:65], v[172:173], s[14:15] op_sel_hi:[1,0]
	v_pk_mul_f32 v[164:165], v[176:177], s[14:15] op_sel_hi:[1,0]
	v_pk_mul_f32 v[166:167], v[174:175], s[14:15] op_sel_hi:[1,0]
	v_lshl_add_u64 v[170:171], v[170:171], 0, s[20:21]
	v_lshl_add_u64 v[170:171], v[170:171], 0, s[12:13]
	v_lshl_add_u64 v[170:171], v[170:171], 0, v[206:207]
	s_waitcnt vmcnt(8)
	v_pk_fma_f32 v[24:25], v[54:55], v[40:41], v[24:25]
	v_pk_fma_f32 v[22:23], v[58:59], v[38:39], v[22:23]
	v_pk_fma_f32 v[28:29], v[60:61], v[44:45], v[28:29]
	v_pk_fma_f32 v[26:27], v[62:63], v[42:43], v[26:27]
	v_pk_fma_f32 v[32:33], v[64:65], v[48:49], v[32:33]
	v_pk_fma_f32 v[30:31], v[162:163], v[46:47], v[30:31]
	v_pk_fma_f32 v[36:37], v[164:165], v[52:53], v[36:37]
	v_pk_fma_f32 v[34:35], v[166:167], v[50:51], v[34:35]
	global_store_dwordx4 v[56:57], v[22:25], off
	global_store_dwordx4 v[56:57], v[26:29], off offset:64
	global_store_dwordx4 v[56:57], v[30:33], off offset:512
	global_store_dwordx4 v[56:57], v[34:37], off offset:576
	global_load_dwordx4 v[22:25], v[170:171], off
	global_load_dwordx4 v[26:29], v[170:171], off offset:64
	global_load_dwordx4 v[30:33], v[170:171], off offset:512
	global_load_dwordx4 v[34:37], v[170:171], off offset:576
	v_pk_mul_f32 v[60:61], v[150:151], s[14:15] op_sel_hi:[1,0]
	v_add_u32_e32 v150, s24, v222
	v_ashrrev_i32_e32 v151, 31, v150
	v_lshlrev_b64 v[150:151], 13, v[150:151]
	v_pk_mul_f32 v[54:55], v[148:149], s[14:15] op_sel_hi:[1,0]
	v_pk_mul_f32 v[56:57], v[146:147], s[14:15] op_sel_hi:[1,0]
	v_pk_mul_f32 v[58:59], v[152:153], s[14:15] op_sel_hi:[1,0]
	v_pk_mul_f32 v[64:65], v[154:155], s[14:15] op_sel_hi:[1,0]
	v_lshl_add_u64 v[152:153], s[0:1], 0, v[150:151]
	v_lshl_add_u64 v[154:155], s[8:9], 0, v[186:187]
	v_pk_mul_f32 v[62:63], v[156:157], s[14:15] op_sel_hi:[1,0]
	v_pk_mul_f32 v[146:147], v[160:161], s[14:15] op_sel_hi:[1,0]
	v_pk_mul_f32 v[148:149], v[158:159], s[14:15] op_sel_hi:[1,0]
	v_lshl_add_u64 v[152:153], v[152:153], 0, s[20:21]
	v_lshl_add_u64 v[154:155], v[154:155], 0, v[2:3]
	v_lshl_add_u64 v[152:153], v[152:153], 0, s[12:13]
	v_lshl_add_u64 v[152:153], v[152:153], 0, v[206:207]
	s_waitcnt vmcnt(8)
;     __device__ __forceinline__ void load(Regs& r, const pg::Unit& u, int g, int wr, int wc, int fr, int fq) const {
;         EPI_G(g)
; #pragma unroll
;         for (int bj = 0; bj < 2; ++bj)
; #pragma unroll
;             for (int n = 0; n < 2; ++n) r.x[bj][n] = *(const f32x4*)(xin + (size_t)row * DM + u.pn * 256 + bj * 128 + wc * 32 + 16 * n + 4 * fq);
;     }
;     __device__ __forceinline__ void finish(const Regs& r, const pg::Acc& acc, const pg::Unit& u, int g, int wr, int wc, int fr, int fq) const {
;         EPI_G(g)
;         const int b = (u.pm * 256) / SEQ;
; #pragma unroll
;         for (int bj = 0; bj < 2; ++bj)
; #pragma unroll
;             for (int n = 0; n < 2; ++n) { const int col = u.pn * 256 + bj * 128 + wc * 32 + 16 * n + 4 * fq;
;                 const f32x4 gv = *(const f32x4*)(gacc + (size_t)b * (NMOD * DM) + col);
;                 *(f32x4*)(xout + (size_t)row * DM + col) = r.x[bj][n] + gv * (acc[ai][bj][m][n] * isc); }
;     }
	v_pk_fma_f32 v[20:21], v[54:55], v[40:41], v[20:21]
	v_pk_fma_f32 v[18:19], v[56:57], v[38:39], v[18:19]
	v_pk_fma_f32 v[16:17], v[58:59], v[44:45], v[16:17]
	v_pk_fma_f32 v[14:15], v[60:61], v[42:43], v[14:15]
	v_pk_fma_f32 v[12:13], v[62:63], v[48:49], v[12:13]
	v_pk_fma_f32 v[10:11], v[64:65], v[46:47], v[10:11]
	v_pk_fma_f32 v[8:9], v[146:147], v[52:53], v[8:9]
	v_pk_fma_f32 v[6:7], v[148:149], v[50:51], v[6:7]
	global_store_dwordx4 v[154:155], v[18:21], off
	global_store_dwordx4 v[154:155], v[14:17], off offset:64
	global_store_dwordx4 v[154:155], v[10:13], off offset:512
	global_store_dwordx4 v[154:155], v[6:9], off offset:576
	global_load_dwordx4 v[6:9], v[152:153], off offset:576
	global_load_dwordx4 v[10:13], v[152:153], off offset:512
	global_load_dwordx4 v[14:17], v[152:153], off offset:64
	global_load_dwordx4 v[18:21], v[152:153], off
	v_pk_mul_f32 v[60:61], v[126:127], s[14:15] op_sel_hi:[1,0]
	v_add_u32_e32 v126, s17, v222
	v_ashrrev_i32_e32 v127, 31, v126
	v_lshlrev_b64 v[126:127], 13, v[126:127]
	v_pk_mul_f32 v[54:55], v[124:125], s[14:15] op_sel_hi:[1,0]
	v_pk_mul_f32 v[56:57], v[122:123], s[14:15] op_sel_hi:[1,0]
	v_pk_mul_f32 v[58:59], v[128:129], s[14:15] op_sel_hi:[1,0]
	v_pk_mul_f32 v[64:65], v[138:139], s[14:15] op_sel_hi:[1,0]
	v_lshl_add_u64 v[128:129], s[0:1], 0, v[126:127]
	v_lshl_add_u64 v[138:139], s[8:9], 0, v[168:169]
	v_pk_mul_f32 v[62:63], v[140:141], s[14:15] op_sel_hi:[1,0]
	v_pk_mul_f32 v[122:123], v[144:145], s[14:15] op_sel_hi:[1,0]
	v_pk_mul_f32 v[124:125], v[142:143], s[14:15] op_sel_hi:[1,0]
	v_lshl_add_u64 v[128:129], v[128:129], 0, s[20:21]
	v_lshl_add_u64 v[138:139], v[138:139], 0, v[2:3]
	v_lshl_add_u64 v[128:129], v[128:129], 0, s[12:13]
	v_lshl_add_u64 v[128:129], v[128:129], 0, v[206:207]
	s_waitcnt vmcnt(8)
	v_pk_fma_f32 v[24:25], v[54:55], v[40:41], v[24:25]
	v_pk_fma_f32 v[22:23], v[56:57], v[38:39], v[22:23]
	v_pk_fma_f32 v[28:29], v[58:59], v[44:45], v[28:29]
	v_pk_fma_f32 v[26:27], v[60:61], v[42:43], v[26:27]
	v_pk_fma_f32 v[32:33], v[62:63], v[48:49], v[32:33]
	v_pk_fma_f32 v[30:31], v[64:65], v[46:47], v[30:31]
	v_pk_fma_f32 v[36:37], v[122:123], v[52:53], v[36:37]
	v_pk_fma_f32 v[34:35], v[124:125], v[50:51], v[34:35]
	global_store_dwordx4 v[138:139], v[22:25], off
	global_store_dwordx4 v[138:139], v[26:29], off offset:64
	global_store_dwordx4 v[138:139], v[30:33], off offset:512
	global_store_dwordx4 v[138:139], v[34:37], off offset:576
	global_load_dwordx4 v[22:25], v[128:129], off
	global_load_dwordx4 v[26:29], v[128:129], off offset:64
	global_load_dwordx4 v[30:33], v[128:129], off offset:512
	global_load_dwordx4 v[34:37], v[128:129], off offset:576
	v_pk_mul_f32 v[58:59], v[120:121], s[14:15] op_sel_hi:[1,0]
	v_add_u32_e32 v120, s22, v222
	v_ashrrev_i32_e32 v121, 31, v120
	v_lshlrev_b64 v[120:121], 13, v[120:121]
	v_pk_mul_f32 v[54:55], v[116:117], s[14:15] op_sel_hi:[1,0]
	v_pk_mul_f32 v[56:57], v[114:115], s[14:15] op_sel_hi:[1,0]
	v_pk_mul_f32 v[60:61], v[118:119], s[14:15] op_sel_hi:[1,0]
	v_lshl_add_u64 v[118:119], s[8:9], 0, v[150:151]
	v_lshl_add_u64 v[122:123], s[0:1], 0, v[120:121]
	v_pk_mul_f32 v[62:63], v[132:133], s[14:15] op_sel_hi:[1,0]
	v_pk_mul_f32 v[64:65], v[130:131], s[14:15] op_sel_hi:[1,0]
	v_pk_mul_f32 v[114:115], v[136:137], s[14:15] op_sel_hi:[1,0]
	v_pk_mul_f32 v[116:117], v[134:135], s[14:15] op_sel_hi:[1,0]
	v_lshl_add_u64 v[118:119], v[118:119], 0, v[2:3]
	v_lshl_add_u64 v[122:123], v[122:123], 0, s[20:21]
	v_lshl_add_u64 v[122:123], v[122:123], 0, s[12:13]
	v_lshl_add_u64 v[122:123], v[122:123], 0, v[206:207]
	s_waitcnt vmcnt(8)
	v_pk_fma_f32 v[20:21], v[54:55], v[40:41], v[20:21]
	v_pk_fma_f32 v[18:19], v[56:57], v[38:39], v[18:19]
	v_pk_fma_f32 v[16:17], v[58:59], v[44:45], v[16:17]
	v_pk_fma_f32 v[14:15], v[60:61], v[42:43], v[14:15]
	v_pk_fma_f32 v[12:13], v[62:63], v[48:49], v[12:13]
	v_pk_fma_f32 v[10:11], v[64:65], v[46:47], v[10:11]
	v_pk_fma_f32 v[8:9], v[114:115], v[52:53], v[8:9]
	v_pk_fma_f32 v[6:7], v[116:117], v[50:51], v[6:7]
	global_store_dwordx4 v[118:119], v[18:21], off
	global_store_dwordx4 v[118:119], v[14:17], off offset:64
	global_store_dwordx4 v[118:119], v[10:13], off offset:512
	global_store_dwordx4 v[118:119], v[6:9], off offset:576
	global_load_dwordx4 v[6:9], v[122:123], off offset:576
	global_load_dwordx4 v[10:13], v[122:123], off offset:512
	global_load_dwordx4 v[14:17], v[122:123], off offset:64
	global_load_dwordx4 v[18:21], v[122:123], off
	v_pk_mul_f32 v[58:59], v[104:105], s[14:15] op_sel_hi:[1,0]
	v_add_u32_e32 v104, s23, v222
	v_ashrrev_i32_e32 v105, 31, v104
	v_lshlrev_b64 v[104:105], 13, v[104:105]
	v_pk_mul_f32 v[54:55], v[100:101], s[14:15] op_sel_hi:[1,0]
	v_pk_mul_f32 v[56:57], v[98:99], s[14:15] op_sel_hi:[1,0]
	v_pk_mul_f32 v[60:61], v[102:103], s[14:15] op_sel_hi:[1,0]
	v_pk_mul_f32 v[64:65], v[106:107], s[14:15] op_sel_hi:[1,0]
	v_lshl_add_u64 v[102:103], s[8:9], 0, v[126:127]
	v_lshl_add_u64 v[106:107], s[0:1], 0, v[104:105]
	v_pk_mul_f32 v[62:63], v[108:109], s[14:15] op_sel_hi:[1,0]
	v_pk_mul_f32 v[98:99], v[112:113], s[14:15] op_sel_hi:[1,0]
	v_pk_mul_f32 v[100:101], v[110:111], s[14:15] op_sel_hi:[1,0]
	v_lshl_add_u64 v[102:103], v[102:103], 0, v[2:3]
	v_lshl_add_u64 v[106:107], v[106:107], 0, s[20:21]
	v_lshl_add_u64 v[106:107], v[106:107], 0, s[12:13]
	v_lshl_add_u64 v[106:107], v[106:107], 0, v[206:207]
	s_waitcnt vmcnt(8)
; template <class P, class MK = NoChain>
; __device__ __forceinline__ void gemm_phase(LAS unsigned char* lds, const P& p, const MK& mk = MK(), bool chain_out = false, bool chained_in = false) {
;     ...
;     if constexpr (!PEEL) {
; #pragma unroll
;         for (int a = 0; a < 2; ++a)
; #pragma unroll
;             for (int b = 0; b < 2; ++b)
; #pragma unroll
;                 for (int m = 0; m < 4; ++m)
; #pragma unroll
;                     for (int n = 0; n < 2; ++n) { typedef double d2_ __attribute__((ext_vector_type(2))); d2_ z_; asm volatile("v_mov_b64 %0, 0" : "=v"(z_.x)); asm volatile("v_mov_b64 %0, 0" : "=v"(z_.y)); acc[a][b][m][n] = __builtin_bit_cast(f32x4, z_); }
;     }
;     __device__ __forceinline__ void load(Regs& r, const pg::Unit& u, int g, int wr, int wc, int fr, int fq) const {
;         EPI_G(g)
; #pragma unroll
;         for (int bj = 0; bj < 2; ++bj)
; #pragma unroll
;             for (int n = 0; n < 2; ++n) r.x[bj][n] = *(const f32x4*)(xin + (size_t)row * DM + u.pn * 256 + bj * 128 + wc * 32 + 16 * n + 4 * fq);
;     }
;     __device__ __forceinline__ void finish(const Regs& r, const pg::Acc& acc, const pg::Unit& u, int g, int wr, int wc, int fr, int fq) const {
;         EPI_G(g)
;         const int b = (u.pm * 256) / SEQ;
; #pragma unroll
;         for (int bj = 0; bj < 2; ++bj)
; #pragma unroll
;             for (int n = 0; n < 2; ++n) { const int col = u.pn * 256 + bj * 128 + wc * 32 + 16 * n + 4 * fq;
;                 const f32x4 gv = *(const f32x4*)(gacc + (size_t)b * (NMOD * DM) + col);
;                 *(f32x4*)(xout + (size_t)row * DM + col) = r.x[bj][n] + gv * (acc[ai][bj][m][n] * isc); }
;     }
	v_pk_fma_f32 v[24:25], v[54:55], v[40:41], v[24:25]
	v_pk_fma_f32 v[22:23], v[56:57], v[38:39], v[22:23]
	v_pk_fma_f32 v[28:29], v[58:59], v[44:45], v[28:29]
	v_pk_fma_f32 v[26:27], v[60:61], v[42:43], v[26:27]
	v_pk_fma_f32 v[32:33], v[62:63], v[48:49], v[32:33]
	v_pk_fma_f32 v[30:31], v[64:65], v[46:47], v[30:31]
	v_pk_fma_f32 v[36:37], v[98:99], v[52:53], v[36:37]
	v_pk_fma_f32 v[34:35], v[100:101], v[50:51], v[34:35]
	global_store_dwordx4 v[102:103], v[22:25], off
	global_store_dwordx4 v[102:103], v[26:29], off offset:64
	global_store_dwordx4 v[102:103], v[30:33], off offset:512
	global_store_dwordx4 v[102:103], v[34:37], off offset:576
	global_load_dwordx4 v[22:25], v[106:107], off
	global_load_dwordx4 v[26:29], v[106:107], off offset:64
	global_load_dwordx4 v[30:33], v[106:107], off offset:512
	global_load_dwordx4 v[34:37], v[106:107], off offset:576
	v_pk_mul_f32 v[54:55], v[84:85], s[14:15] op_sel_hi:[1,0]
	v_pk_mul_f32 v[56:57], v[82:83], s[14:15] op_sel_hi:[1,0]
	v_pk_mul_f32 v[60:61], v[86:87], s[14:15] op_sel_hi:[1,0]
	v_lshl_add_u64 v[86:87], s[8:9], 0, v[120:121]
	v_pk_mul_f32 v[58:59], v[88:89], s[14:15] op_sel_hi:[1,0]
	v_pk_mul_f32 v[62:63], v[92:93], s[14:15] op_sel_hi:[1,0]
	v_pk_mul_f32 v[64:65], v[90:91], s[14:15] op_sel_hi:[1,0]
	v_pk_mul_f32 v[82:83], v[96:97], s[14:15] op_sel_hi:[1,0]
	v_pk_mul_f32 v[84:85], v[94:95], s[14:15] op_sel_hi:[1,0]
	v_lshl_add_u64 v[86:87], v[86:87], 0, v[2:3]
	s_waitcnt vmcnt(8)
	v_pk_fma_f32 v[20:21], v[54:55], v[40:41], v[20:21]
	v_pk_fma_f32 v[18:19], v[56:57], v[38:39], v[18:19]
	v_pk_fma_f32 v[16:17], v[58:59], v[44:45], v[16:17]
	v_pk_fma_f32 v[14:15], v[60:61], v[42:43], v[14:15]
	v_pk_fma_f32 v[12:13], v[62:63], v[48:49], v[12:13]
	v_pk_fma_f32 v[10:11], v[64:65], v[46:47], v[10:11]
	v_pk_fma_f32 v[8:9], v[82:83], v[52:53], v[8:9]
	v_pk_fma_f32 v[6:7], v[84:85], v[50:51], v[6:7]
	global_store_dwordx4 v[86:87], v[18:21], off
	global_store_dwordx4 v[86:87], v[14:17], off offset:64
	global_store_dwordx4 v[86:87], v[10:13], off offset:512
	global_store_dwordx4 v[86:87], v[6:9], off offset:576
	global_load_dwordx4 v[6:9], v[4:5], off
	global_load_dwordx4 v[10:13], v[4:5], off offset:64
	global_load_dwordx4 v[14:17], v[4:5], off offset:512
	global_load_dwordx4 v[18:21], v[4:5], off offset:576
	v_pk_mul_f32 v[4:5], v[68:69], s[14:15] op_sel_hi:[1,0]
	v_pk_mul_f32 v[38:39], v[66:67], s[14:15] op_sel_hi:[1,0]
	v_lshl_add_u64 v[52:53], s[8:9], 0, v[104:105]
	v_pk_mul_f32 v[40:41], v[72:73], s[14:15] op_sel_hi:[1,0]
	v_pk_mul_f32 v[42:43], v[70:71], s[14:15] op_sel_hi:[1,0]
	v_pk_mul_f32 v[44:45], v[76:77], s[14:15] op_sel_hi:[1,0]
	v_pk_mul_f32 v[46:47], v[74:75], s[14:15] op_sel_hi:[1,0]
	v_pk_mul_f32 v[48:49], v[80:81], s[14:15] op_sel_hi:[1,0]
	v_pk_mul_f32 v[50:51], v[78:79], s[14:15] op_sel_hi:[1,0]
	v_lshl_add_u64 v[52:53], v[52:53], 0, v[2:3]
	s_waitcnt vmcnt(0)
	v_pk_fma_f32 v[4:5], v[4:5], v[8:9], v[24:25]
	v_pk_fma_f32 v[2:3], v[38:39], v[6:7], v[22:23]
	v_pk_fma_f32 v[8:9], v[40:41], v[12:13], v[28:29]
	v_pk_fma_f32 v[6:7], v[42:43], v[10:11], v[26:27]
	v_pk_fma_f32 v[12:13], v[44:45], v[16:17], v[32:33]
	v_pk_fma_f32 v[10:11], v[46:47], v[14:15], v[30:31]
	v_pk_fma_f32 v[16:17], v[48:49], v[20:21], v[36:37]
	v_pk_fma_f32 v[14:15], v[50:51], v[18:19], v[34:35]
	global_store_dwordx4 v[52:53], v[2:5], off
	global_store_dwordx4 v[52:53], v[6:9], off offset:64
	global_store_dwordx4 v[52:53], v[10:13], off offset:512
	global_store_dwordx4 v[52:53], v[14:17], off offset:576
	s_cbranch_vccnz .LBB0_1252
	s_mov_b64 s[2:3], 0
	v_mov_b64 v[178:179], 0
	v_mov_b64 v[180:181], 0
	v_mov_b64 v[182:183], 0
	v_mov_b64 v[184:185], 0
	v_mov_b64 v[162:163], 0
	v_mov_b64 v[164:165], 0
	v_mov_b64 v[166:167], 0
	v_mov_b64 v[168:169], 0
	v_mov_b64 v[146:147], 0
	v_mov_b64 v[148:149], 0
	v_mov_b64 v[150:151], 0
	v_mov_b64 v[152:153], 0
	v_mov_b64 v[122:123], 0
	v_mov_b64 v[124:125], 0
	v_mov_b64 v[126:127], 0
	v_mov_b64 v[128:129], 0
	v_mov_b64 v[186:187], 0
	v_mov_b64 v[188:189], 0
	v_mov_b64 v[190:191], 0
	v_mov_b64 v[192:193], 0
	v_mov_b64 v[170:171], 0
	v_mov_b64 v[172:173], 0
	v_mov_b64 v[174:175], 0
	v_mov_b64 v[176:177], 0
	v_mov_b64 v[154:155], 0
	v_mov_b64 v[156:157], 0
	v_mov_b64 v[158:159], 0
	v_mov_b64 v[160:161], 0
	v_mov_b64 v[138:139], 0
	v_mov_b64 v[140:141], 0
	v_mov_b64 v[142:143], 0
	v_mov_b64 v[144:145], 0
	v_mov_b64 v[114:115], 0
	v_mov_b64 v[116:117], 0
	v_mov_b64 v[118:119], 0
	v_mov_b64 v[120:121], 0
	v_mov_b64 v[98:99], 0
	v_mov_b64 v[100:101], 0
	v_mov_b64 v[102:103], 0
	v_mov_b64 v[104:105], 0
	v_mov_b64 v[82:83], 0
	v_mov_b64 v[84:85], 0
	v_mov_b64 v[86:87], 0
	v_mov_b64 v[88:89], 0
	v_mov_b64 v[66:67], 0
	v_mov_b64 v[68:69], 0
	v_mov_b64 v[70:71], 0
	v_mov_b64 v[72:73], 0
	v_mov_b64 v[130:131], 0
	v_mov_b64 v[132:133], 0
	v_mov_b64 v[134:135], 0
	v_mov_b64 v[136:137], 0
	v_mov_b64 v[106:107], 0
	v_mov_b64 v[108:109], 0
	v_mov_b64 v[110:111], 0
	v_mov_b64 v[112:113], 0
	v_mov_b64 v[90:91], 0
	v_mov_b64 v[92:93], 0
	v_mov_b64 v[94:95], 0
	v_mov_b64 v[96:97], 0
	v_mov_b64 v[74:75], 0
	v_mov_b64 v[76:77], 0
	v_mov_b64 v[78:79], 0
	v_mov_b64 v[80:81], 0
	s_branch .LBB0_1252

; __device__ __forceinline__ int otid() { int t = threadIdx.x; asm volatile("" : "+v"(t)); return t; }
;     __device__ __forceinline__ void a_offsets(const pg::Unit& u, unsigned (&off)[2][2]) const {
;         int R[2], C[2]; { const int t_ = otid(); pg::stage_rc(t_ * 16, R[0], C[0]); pg::stage_rc(t_ * 16 + 8192, R[1], C[1]); }
;         if (u.aux < 64) {
;             const int n = T.cnt[u.aux]; const int* lp = LIST + (size_t)u.aux * NT + u.pm * 256;
; #pragma unroll
;             for (int h = 0; h < 2; ++h)
; #pragma unroll
;                 for (int i = 0; i < 2; ++i) { const int r = R[i] + 128 * h; const int tok = (u.pm * 256 + r < n) ? lp[r] : 0; off[h][i] = (unsigned)(tok * K + C[i] * 2); }
;         } else {
; #pragma unroll
;             for (int h = 0; h < 2; ++h)
; #pragma unroll
;                 for (int i = 0; i < 2; ++i) off[h][i] = (unsigned)((u.pm * 256 + R[i] + 128 * h) * K + C[i] * 2);
;         }
.LBB0_1454:
.LBB0_1455:
	s_lshl_b32 s0, s28, 2
	s_add_i32 s0, s0, 0
	s_add_i32 s0, s0, 0x20100
	v_mov_b32_e32 v3, s0
	ds_read_b32 v13, v3
	s_mov_b32 s29, 0
	s_lshl_b64 s[0:1], s[28:29], 15
	v_lshlrev_b32_e32 v8, 8, v1
	s_add_u32 s0, s49, s0
	v_ashrrev_i32_e32 v9, 31, v8
	s_addc_u32 s1, s50, s1
	v_lshlrev_b64 v[6:7], 2, v[8:9]
	v_add_u32_e32 v14, v4, v8
	v_lshl_add_u64 v[6:7], s[0:1], 0, v[6:7]
	v_ashrrev_i32_e32 v5, 31, v4
	v_ashrrev_i32_e32 v3, 31, v2
	v_add_u32_e32 v15, v2, v8
	v_lshl_add_u64 v[4:5], v[4:5], 2, v[6:7]
	v_lshl_add_u64 v[2:3], v[2:3], 2, v[6:7]
	global_load_dword v9, v[4:5], off
	global_load_dword v1, v[2:3], off
	global_load_dword v16, v[4:5], off offset:512
	global_load_dword v17, v[2:3], off offset:512
	s_waitcnt lgkmcnt(0)
	v_cmp_lt_i32_e64 s[0:1], v14, v13
	v_add_u32_e32 v14, 0x80, v14
	s_waitcnt vmcnt(0)
	v_cndmask_b32_e64 v9, 0, v9, s[0:1]
	v_cmp_lt_i32_e32 vcc, v15, v13
	v_add_u32_e32 v15, 0x80, v15
	s_nop 0
	v_cndmask_b32_e32 v1, 0, v1, vcc
	v_cmp_lt_i32_e64 s[0:1], v14, v13
	v_lshlrev_b32_e32 v9, 11, v9
	v_lshlrev_b32_e32 v1, 11, v1
	v_cndmask_b32_e64 v16, 0, v16, s[0:1]
	v_cmp_lt_i32_e32 vcc, v15, v13
	v_lshlrev_b32_e32 v16, 11, v16
	s_nop 0
	v_cndmask_b32_e32 v14, 0, v17, vcc
	v_lshlrev_b32_e32 v14, 11, v14
	v_mov_b32_e32 v15, v16
	v_or_b32_e32 v222, v15, v12
	v_or_b32_e32 v220, v1, v12
	v_or_b32_e32 v210, v9, v12
	v_or_b32_e32 v224, v14, v12

; __device__ __forceinline__ int otid() { int t = threadIdx.x; asm volatile("" : "+v"(t)); return t; }
; template <class P, class MK = NoChain>
; __device__ __forceinline__ void gemm_phase(LAS unsigned char* lds, const P& p, const MK& mk = MK(), bool chain_out = false, bool chained_in = false) {
;     ...
;                 if (last && has_next) p.a_offsets(nxt, nvA);
;     __device__ __forceinline__ void a_offsets(const pg::Unit& u, unsigned (&off)[2][2]) const {
;         int R[2], C[2]; { const int t_ = otid(); pg::stage_rc(t_ * 16, R[0], C[0]); pg::stage_rc(t_ * 16 + 8192, R[1], C[1]); }
;         if (u.aux < 64) {
;             const int n = T.cnt[u.aux]; const int* lp = LIST + (size_t)u.aux * NT + u.pm * 256;
; #pragma unroll
;             for (int h = 0; h < 2; ++h)
; #pragma unroll
;                 for (int i = 0; i < 2; ++i) { const int r = R[i] + 128 * h; const int tok = (u.pm * 256 + r < n) ? lp[r] : 0; off[h][i] = (unsigned)(tok * K + C[i] * 2); }
;         } else {
; #pragma unroll
;             for (int h = 0; h < 2; ++h)
; #pragma unroll
;                 for (int i = 0; i < 2; ++i) off[h][i] = (unsigned)((u.pm * 256 + R[i] + 128 * h) * K + C[i] * 2);
;         }
.LBB0_1495:
	s_andn2_b64 vcc, exec, s[40:41]
	s_cbranch_vccnz .LBB0_1505
	v_mov_b32_e32 v13, s25
	ds_read_b32 v9, v13
	v_add_u32_e32 v10, v4, v194
	v_add_u32_e32 v11, v2, v194
	v_ashrrev_i32_e32 v5, 31, v4
	v_ashrrev_i32_e32 v3, 31, v2
	v_lshl_add_u64 v[4:5], v[4:5], 2, v[196:197]
	v_lshl_add_u64 v[2:3], v[2:3], 2, v[196:197]
	global_load_dword v8, v[4:5], off
	global_load_dword v7, v[2:3], off
	global_load_dword v12, v[4:5], off offset:512
	global_load_dword v13, v[2:3], off offset:512
	s_waitcnt lgkmcnt(0)
	v_cmp_lt_i32_e64 s[40:41], v10, v9
	v_add_u32_e32 v10, 0x80, v10
	s_waitcnt vmcnt(0)
	v_cndmask_b32_e64 v8, 0, v8, s[40:41]
	v_cmp_lt_i32_e32 vcc, v11, v9
	v_add_u32_e32 v11, 0x80, v11
	s_nop 0
	v_cndmask_b32_e32 v7, 0, v7, vcc
	v_cmp_lt_i32_e64 s[40:41], v10, v9
	v_lshlrev_b32_e32 v8, 11, v8
	v_lshlrev_b32_e32 v7, 11, v7
	v_cndmask_b32_e64 v12, 0, v12, s[40:41]
	v_cmp_lt_i32_e32 vcc, v11, v9
	v_lshlrev_b32_e32 v12, 11, v12
	s_nop 0
	v_cndmask_b32_e32 v10, 0, v13, vcc
	v_lshlrev_b32_e32 v10, 11, v10
	v_or_b32_e32 v241, v12, v6
	v_or_b32_e32 v210, v7, v6
	v_or_b32_e32 v240, v8, v6
	v_or_b32_e32 v218, v10, v6

;     __device__ __forceinline__ void load(Regs& r, const pg::Unit& u, int g, int wr, int wc, int fr, int fq) const {
;         EPI_G(g)
; #pragma unroll
;         for (int bj = 0; bj < 2; ++bj)
; #pragma unroll
;             for (int n = 0; n < 2; ++n) r.x[bj][n] = *(const f32x4*)(xin + (size_t)row * DM + u.pn * 256 + bj * 128 + wc * 32 + 16 * n + 4 * fq);
;     }
;     __device__ __forceinline__ void finish(const Regs& r, const pg::Acc& acc, const pg::Unit& u, int g, int wr, int wc, int fr, int fq) const {
;         EPI_G(g)
;         const int b = (u.pm * 256) / SEQ;
; #pragma unroll
;         for (int bj = 0; bj < 2; ++bj)
; #pragma unroll
;             for (int n = 0; n < 2; ++n) { const int col = u.pn * 256 + bj * 128 + wc * 32 + 16 * n + 4 * fq;
;                 const f32x4 gv = *(const f32x4*)(gacc + (size_t)b * (NMOD * DM) + col);
;                 *(f32x4*)(xout + (size_t)row * DM + col) = r.x[bj][n] + gv * (acc[ai][bj][m][n] * isc); }
;     }
.LBB0_2540:
	s_lshl_b32 s22, s33, 8
	v_add_u32_e32 v2, s22, v1
	v_ashrrev_i32_e32 v3, 31, v2
	s_lshl_b32 s20, s18, 8
	v_lshlrev_b64 v[2:3], 13, v[2:3]
	s_ashr_i32 s21, s20, 31
	v_lshl_add_u64 v[54:55], s[6:7], 0, v[2:3]
	s_lshl_b64 s[18:19], s[20:21], 2
	v_lshl_add_u64 v[2:3], v[54:55], 0, s[18:19]
	s_mov_b32 s11, s5
	v_lshl_add_u64 v[2:3], v[2:3], 0, s[10:11]
	v_mov_b32_e32 v207, v199
	v_lshl_add_u64 v[2:3], v[2:3], 0, v[206:207]
	s_or_b32 s15, s22, 16
	global_load_dwordx4 v[6:9], v[2:3], off
	global_load_dwordx4 v[10:13], v[2:3], off offset:64
	global_load_dwordx4 v[14:17], v[2:3], off offset:512
	global_load_dwordx4 v[18:21], v[2:3], off offset:576
	v_add_u32_e32 v2, s15, v1
	v_ashrrev_i32_e32 v3, 31, v2
	v_lshlrev_b64 v[2:3], 13, v[2:3]
	v_lshl_add_u64 v[56:57], s[6:7], 0, v[2:3]
	s_ashr_i32 s21, s33, 31
	v_lshl_add_u64 v[2:3], v[56:57], 0, s[18:19]
	s_lshr_b32 s21, s21, 28
	v_lshl_add_u64 v[2:3], v[2:3], 0, s[10:11]
	s_add_i32 s21, s33, s21
	v_lshl_add_u64 v[2:3], v[2:3], 0, v[206:207]
	s_ashr_i32 s21, s21, 4
	global_load_dwordx4 v[22:25], v[2:3], off
	global_load_dwordx4 v[26:29], v[2:3], off offset:64
	global_load_dwordx4 v[30:33], v[2:3], off offset:512
	global_load_dwordx4 v[34:37], v[2:3], off offset:576
	s_mul_hi_i32 s23, s21, 0xc000
	s_mul_i32 s21, s21, 0xc000
	v_or_b32_e32 v2, s20, v221
	s_add_u32 s20, s42, s21
	v_ashrrev_i32_e32 v3, 31, v2
	s_addc_u32 s21, s43, s23
	v_lshlrev_b64 v[2:3], 2, v[2:3]
	v_lshl_add_u64 v[4:5], s[20:21], 0, v[2:3]
	global_load_dwordx4 v[38:41], v[4:5], off
	global_load_dwordx4 v[42:45], v[4:5], off offset:64
	global_load_dwordx4 v[46:49], v[4:5], off offset:512
	global_load_dwordx4 v[50:53], v[4:5], off offset:576
	s_or_b32 s20, s22, 32
	v_pk_mul_f32 v[58:59], v[180:181], s[12:13] op_sel_hi:[1,0]
	v_pk_mul_f32 v[180:181], v[186:187], s[12:13] op_sel_hi:[1,0]
	v_add_u32_e32 v186, s20, v1
	v_ashrrev_i32_e32 v187, 31, v186
	v_lshlrev_b64 v[186:187], 13, v[186:187]
	v_pk_mul_f32 v[60:61], v[178:179], s[12:13] op_sel_hi:[1,0]
	v_lshl_add_u64 v[186:187], s[6:7], 0, v[186:187]
	v_pk_mul_f32 v[62:63], v[184:185], s[12:13] op_sel_hi:[1,0]
	v_pk_mul_f32 v[64:65], v[182:183], s[12:13] op_sel_hi:[1,0]
	v_pk_mul_f32 v[178:179], v[188:189], s[12:13] op_sel_hi:[1,0]
	v_pk_mul_f32 v[182:183], v[192:193], s[12:13] op_sel_hi:[1,0]
	v_pk_mul_f32 v[184:185], v[190:191], s[12:13] op_sel_hi:[1,0]
	v_lshl_add_u64 v[54:55], v[54:55], 0, v[2:3]
	v_lshl_add_u64 v[188:189], v[186:187], 0, s[18:19]
	v_lshl_add_u64 v[188:189], v[188:189], 0, s[10:11]
	v_lshl_add_u64 v[188:189], v[188:189], 0, v[206:207]
	s_or_b32 s21, s22, 48
	v_lshl_add_u64 v[56:57], v[56:57], 0, v[2:3]
	s_andn2_b64 vcc, exec, s[2:3]
	s_mov_b64 s[2:3], -1
	s_waitcnt vmcnt(0)
	v_pk_fma_f32 v[8:9], v[58:59], v[40:41], v[8:9]
	v_pk_fma_f32 v[6:7], v[60:61], v[38:39], v[6:7]
	v_pk_fma_f32 v[12:13], v[62:63], v[44:45], v[12:13]
	v_pk_fma_f32 v[10:11], v[64:65], v[42:43], v[10:11]
	v_pk_fma_f32 v[16:17], v[178:179], v[48:49], v[16:17]
	v_pk_fma_f32 v[14:15], v[180:181], v[46:47], v[14:15]
	v_pk_fma_f32 v[20:21], v[182:183], v[52:53], v[20:21]
	v_pk_fma_f32 v[18:19], v[184:185], v[50:51], v[18:19]
	global_store_dwordx4 v[54:55], v[6:9], off
	global_store_dwordx4 v[54:55], v[10:13], off offset:64
	global_store_dwordx4 v[54:55], v[14:17], off offset:512
	global_store_dwordx4 v[54:55], v[18:21], off offset:576
	global_load_dwordx4 v[6:9], v[188:189], off offset:576
	global_load_dwordx4 v[10:13], v[188:189], off offset:512
	global_load_dwordx4 v[14:17], v[188:189], off offset:64
	global_load_dwordx4 v[18:21], v[188:189], off
	v_pk_mul_f32 v[60:61], v[168:169], s[12:13] op_sel_hi:[1,0]
	v_add_u32_e32 v168, s21, v1
	v_ashrrev_i32_e32 v169, 31, v168
	v_lshlrev_b64 v[168:169], 13, v[168:169]
	v_pk_mul_f32 v[54:55], v[164:165], s[12:13] op_sel_hi:[1,0]
	v_pk_mul_f32 v[58:59], v[162:163], s[12:13] op_sel_hi:[1,0]
	v_lshl_add_u64 v[168:169], s[6:7], 0, v[168:169]
	v_pk_mul_f32 v[62:63], v[166:167], s[12:13] op_sel_hi:[1,0]
	v_pk_mul_f32 v[64:65], v[172:173], s[12:13] op_sel_hi:[1,0]
	v_pk_mul_f32 v[162:163], v[170:171], s[12:13] op_sel_hi:[1,0]
	v_pk_mul_f32 v[164:165], v[176:177], s[12:13] op_sel_hi:[1,0]
	v_pk_mul_f32 v[166:167], v[174:175], s[12:13] op_sel_hi:[1,0]
	v_lshl_add_u64 v[170:171], v[168:169], 0, s[18:19]
	v_lshl_add_u64 v[170:171], v[170:171], 0, s[10:11]
	v_lshl_add_u64 v[170:171], v[170:171], 0, v[206:207]
	s_waitcnt vmcnt(8)
	v_pk_fma_f32 v[24:25], v[54:55], v[40:41], v[24:25]
	v_pk_fma_f32 v[22:23], v[58:59], v[38:39], v[22:23]
	v_pk_fma_f32 v[28:29], v[60:61], v[44:45], v[28:29]
	v_pk_fma_f32 v[26:27], v[62:63], v[42:43], v[26:27]
	v_pk_fma_f32 v[32:33], v[64:65], v[48:49], v[32:33]
	v_pk_fma_f32 v[30:31], v[162:163], v[46:47], v[30:31]
	v_pk_fma_f32 v[36:37], v[164:165], v[52:53], v[36:37]
	v_pk_fma_f32 v[34:35], v[166:167], v[50:51], v[34:35]
	global_store_dwordx4 v[56:57], v[22:25], off
	global_store_dwordx4 v[56:57], v[26:29], off offset:64
	global_store_dwordx4 v[56:57], v[30:33], off offset:512
	global_store_dwordx4 v[56:57], v[34:37], off offset:576
	global_load_dwordx4 v[22:25], v[170:171], off
	global_load_dwordx4 v[26:29], v[170:171], off offset:64
	global_load_dwordx4 v[30:33], v[170:171], off offset:512
	global_load_dwordx4 v[34:37], v[170:171], off offset:576
	v_pk_mul_f32 v[60:61], v[150:151], s[12:13] op_sel_hi:[1,0]
	v_add_u32_e32 v150, s22, v222
	v_ashrrev_i32_e32 v151, 31, v150
	v_lshlrev_b64 v[150:151], 13, v[150:151]
	v_pk_mul_f32 v[54:55], v[148:149], s[12:13] op_sel_hi:[1,0]
	v_pk_mul_f32 v[56:57], v[146:147], s[12:13] op_sel_hi:[1,0]
	v_lshl_add_u64 v[150:151], s[6:7], 0, v[150:151]
	v_pk_mul_f32 v[58:59], v[152:153], s[12:13] op_sel_hi:[1,0]
	v_pk_mul_f32 v[62:63], v[156:157], s[12:13] op_sel_hi:[1,0]
	v_pk_mul_f32 v[64:65], v[154:155], s[12:13] op_sel_hi:[1,0]
	v_pk_mul_f32 v[146:147], v[160:161], s[12:13] op_sel_hi:[1,0]
	v_pk_mul_f32 v[148:149], v[158:159], s[12:13] op_sel_hi:[1,0]
	v_lshl_add_u64 v[152:153], v[150:151], 0, s[18:19]
	v_lshl_add_u64 v[154:155], v[186:187], 0, v[2:3]
	v_lshl_add_u64 v[152:153], v[152:153], 0, s[10:11]
	v_lshl_add_u64 v[152:153], v[152:153], 0, v[206:207]
	s_waitcnt vmcnt(8)
;     __device__ __forceinline__ void load(Regs& r, const pg::Unit& u, int g, int wr, int wc, int fr, int fq) const {
;         EPI_G(g)
; #pragma unroll
;         for (int bj = 0; bj < 2; ++bj)
; #pragma unroll
;             for (int n = 0; n < 2; ++n) r.x[bj][n] = *(const f32x4*)(xin + (size_t)row * DM + u.pn * 256 + bj * 128 + wc * 32 + 16 * n + 4 * fq);
;     }
;     __device__ __forceinline__ void finish(const Regs& r, const pg::Acc& acc, const pg::Unit& u, int g, int wr, int wc, int fr, int fq) const {
;         EPI_G(g)
;         const int b = (u.pm * 256) / SEQ;
; #pragma unroll
;         for (int bj = 0; bj < 2; ++bj)
; #pragma unroll
;             for (int n = 0; n < 2; ++n) { const int col = u.pn * 256 + bj * 128 + wc * 32 + 16 * n + 4 * fq;
;                 const f32x4 gv = *(const f32x4*)(gacc + (size_t)b * (NMOD * DM) + col);
;                 *(f32x4*)(xout + (size_t)row * DM + col) = r.x[bj][n] + gv * (acc[ai][bj][m][n] * isc); }
;     }
	v_pk_fma_f32 v[20:21], v[54:55], v[40:41], v[20:21]
	v_pk_fma_f32 v[18:19], v[56:57], v[38:39], v[18:19]
	v_pk_fma_f32 v[16:17], v[58:59], v[44:45], v[16:17]
	v_pk_fma_f32 v[14:15], v[60:61], v[42:43], v[14:15]
	v_pk_fma_f32 v[12:13], v[62:63], v[48:49], v[12:13]
	v_pk_fma_f32 v[10:11], v[64:65], v[46:47], v[10:11]
	v_pk_fma_f32 v[8:9], v[146:147], v[52:53], v[8:9]
	v_pk_fma_f32 v[6:7], v[148:149], v[50:51], v[6:7]
	global_store_dwordx4 v[154:155], v[18:21], off
	global_store_dwordx4 v[154:155], v[14:17], off offset:64
	global_store_dwordx4 v[154:155], v[10:13], off offset:512
	global_store_dwordx4 v[154:155], v[6:9], off offset:576
	global_load_dwordx4 v[6:9], v[152:153], off offset:576
	global_load_dwordx4 v[10:13], v[152:153], off offset:512
	global_load_dwordx4 v[14:17], v[152:153], off offset:64
	global_load_dwordx4 v[18:21], v[152:153], off
	v_pk_mul_f32 v[60:61], v[126:127], s[12:13] op_sel_hi:[1,0]
	v_add_u32_e32 v126, s15, v222
	v_ashrrev_i32_e32 v127, 31, v126
	v_lshlrev_b64 v[126:127], 13, v[126:127]
	v_pk_mul_f32 v[54:55], v[124:125], s[12:13] op_sel_hi:[1,0]
	v_pk_mul_f32 v[56:57], v[122:123], s[12:13] op_sel_hi:[1,0]
	v_lshl_add_u64 v[126:127], s[6:7], 0, v[126:127]
	v_pk_mul_f32 v[58:59], v[128:129], s[12:13] op_sel_hi:[1,0]
	v_pk_mul_f32 v[62:63], v[140:141], s[12:13] op_sel_hi:[1,0]
	v_pk_mul_f32 v[64:65], v[138:139], s[12:13] op_sel_hi:[1,0]
	v_pk_mul_f32 v[122:123], v[144:145], s[12:13] op_sel_hi:[1,0]
	v_pk_mul_f32 v[124:125], v[142:143], s[12:13] op_sel_hi:[1,0]
	v_lshl_add_u64 v[128:129], v[126:127], 0, s[18:19]
	v_lshl_add_u64 v[138:139], v[168:169], 0, v[2:3]
	v_lshl_add_u64 v[128:129], v[128:129], 0, s[10:11]
	v_lshl_add_u64 v[128:129], v[128:129], 0, v[206:207]
	s_waitcnt vmcnt(8)
	v_pk_fma_f32 v[24:25], v[54:55], v[40:41], v[24:25]
	v_pk_fma_f32 v[22:23], v[56:57], v[38:39], v[22:23]
	v_pk_fma_f32 v[28:29], v[58:59], v[44:45], v[28:29]
	v_pk_fma_f32 v[26:27], v[60:61], v[42:43], v[26:27]
	v_pk_fma_f32 v[32:33], v[62:63], v[48:49], v[32:33]
	v_pk_fma_f32 v[30:31], v[64:65], v[46:47], v[30:31]
	v_pk_fma_f32 v[36:37], v[122:123], v[52:53], v[36:37]
	v_pk_fma_f32 v[34:35], v[124:125], v[50:51], v[34:35]
	global_store_dwordx4 v[138:139], v[22:25], off
	global_store_dwordx4 v[138:139], v[26:29], off offset:64
	global_store_dwordx4 v[138:139], v[30:33], off offset:512
	global_store_dwordx4 v[138:139], v[34:37], off offset:576
	global_load_dwordx4 v[22:25], v[128:129], off
	global_load_dwordx4 v[26:29], v[128:129], off offset:64
	global_load_dwordx4 v[30:33], v[128:129], off offset:512
	global_load_dwordx4 v[34:37], v[128:129], off offset:576
	v_pk_mul_f32 v[58:59], v[120:121], s[12:13] op_sel_hi:[1,0]
	v_add_u32_e32 v120, s20, v222
	v_ashrrev_i32_e32 v121, 31, v120
	v_lshlrev_b64 v[120:121], 13, v[120:121]
	v_pk_mul_f32 v[54:55], v[116:117], s[12:13] op_sel_hi:[1,0]
	v_pk_mul_f32 v[56:57], v[114:115], s[12:13] op_sel_hi:[1,0]
	v_lshl_add_u64 v[120:121], s[6:7], 0, v[120:121]
	v_pk_mul_f32 v[60:61], v[118:119], s[12:13] op_sel_hi:[1,0]
	v_pk_mul_f32 v[62:63], v[132:133], s[12:13] op_sel_hi:[1,0]
	v_pk_mul_f32 v[64:65], v[130:131], s[12:13] op_sel_hi:[1,0]
	v_pk_mul_f32 v[114:115], v[136:137], s[12:13] op_sel_hi:[1,0]
	v_pk_mul_f32 v[116:117], v[134:135], s[12:13] op_sel_hi:[1,0]
	v_lshl_add_u64 v[118:119], v[150:151], 0, v[2:3]
	v_lshl_add_u64 v[122:123], v[120:121], 0, s[18:19]
	v_lshl_add_u64 v[122:123], v[122:123], 0, s[10:11]
	v_lshl_add_u64 v[122:123], v[122:123], 0, v[206:207]
	s_waitcnt vmcnt(8)
	v_pk_fma_f32 v[20:21], v[54:55], v[40:41], v[20:21]
	v_pk_fma_f32 v[18:19], v[56:57], v[38:39], v[18:19]
	v_pk_fma_f32 v[16:17], v[58:59], v[44:45], v[16:17]
	v_pk_fma_f32 v[14:15], v[60:61], v[42:43], v[14:15]
	v_pk_fma_f32 v[12:13], v[62:63], v[48:49], v[12:13]
	v_pk_fma_f32 v[10:11], v[64:65], v[46:47], v[10:11]
	v_pk_fma_f32 v[8:9], v[114:115], v[52:53], v[8:9]
	v_pk_fma_f32 v[6:7], v[116:117], v[50:51], v[6:7]
	global_store_dwordx4 v[118:119], v[18:21], off
	global_store_dwordx4 v[118:119], v[14:17], off offset:64
	global_store_dwordx4 v[118:119], v[10:13], off offset:512
	global_store_dwordx4 v[118:119], v[6:9], off offset:576
	global_load_dwordx4 v[6:9], v[122:123], off offset:576
	global_load_dwordx4 v[10:13], v[122:123], off offset:512
	global_load_dwordx4 v[14:17], v[122:123], off offset:64
	global_load_dwordx4 v[18:21], v[122:123], off
	v_pk_mul_f32 v[58:59], v[104:105], s[12:13] op_sel_hi:[1,0]
	v_add_u32_e32 v104, s21, v222
	v_ashrrev_i32_e32 v105, 31, v104
	v_lshlrev_b64 v[104:105], 13, v[104:105]
	v_pk_mul_f32 v[54:55], v[100:101], s[12:13] op_sel_hi:[1,0]
	v_pk_mul_f32 v[56:57], v[98:99], s[12:13] op_sel_hi:[1,0]
	v_lshl_add_u64 v[104:105], s[6:7], 0, v[104:105]
	v_pk_mul_f32 v[60:61], v[102:103], s[12:13] op_sel_hi:[1,0]
	v_pk_mul_f32 v[62:63], v[108:109], s[12:13] op_sel_hi:[1,0]
	v_pk_mul_f32 v[64:65], v[106:107], s[12:13] op_sel_hi:[1,0]
	v_pk_mul_f32 v[98:99], v[112:113], s[12:13] op_sel_hi:[1,0]
	v_pk_mul_f32 v[100:101], v[110:111], s[12:13] op_sel_hi:[1,0]
	v_lshl_add_u64 v[102:103], v[126:127], 0, v[2:3]
	v_lshl_add_u64 v[106:107], v[104:105], 0, s[18:19]
	v_lshl_add_u64 v[106:107], v[106:107], 0, s[10:11]
	v_lshl_add_u64 v[106:107], v[106:107], 0, v[206:207]
	s_waitcnt vmcnt(8)
; template <class P, class MK = NoChain>
; __device__ __forceinline__ void gemm_phase(LAS unsigned char* lds, const P& p, const MK& mk = MK(), bool chain_out = false, bool chained_in = false) {
;     ...
;     if constexpr (!PEEL) {
; #pragma unroll
;         for (int a = 0; a < 2; ++a)
; #pragma unroll
;             for (int b = 0; b < 2; ++b)
; #pragma unroll
;                 for (int m = 0; m < 4; ++m)
; #pragma unroll
;                     for (int n = 0; n < 2; ++n) { typedef double d2_ __attribute__((ext_vector_type(2))); d2_ z_; asm volatile("v_mov_b64 %0, 0" : "=v"(z_.x)); asm volatile("v_mov_b64 %0, 0" : "=v"(z_.y)); acc[a][b][m][n] = __builtin_bit_cast(f32x4, z_); }
;     }
;     __device__ __forceinline__ void load(Regs& r, const pg::Unit& u, int g, int wr, int wc, int fr, int fq) const {
;         EPI_G(g)
; #pragma unroll
;         for (int bj = 0; bj < 2; ++bj)
; #pragma unroll
;             for (int n = 0; n < 2; ++n) r.x[bj][n] = *(const f32x4*)(xin + (size_t)row * DM + u.pn * 256 + bj * 128 + wc * 32 + 16 * n + 4 * fq);
;     }
;     __device__ __forceinline__ void finish(const Regs& r, const pg::Acc& acc, const pg::Unit& u, int g, int wr, int wc, int fr, int fq) const {
;         EPI_G(g)
;         const int b = (u.pm * 256) / SEQ;
; #pragma unroll
;         for (int bj = 0; bj < 2; ++bj)
; #pragma unroll
;             for (int n = 0; n < 2; ++n) { const int col = u.pn * 256 + bj * 128 + wc * 32 + 16 * n + 4 * fq;
;                 const f32x4 gv = *(const f32x4*)(gacc + (size_t)b * (NMOD * DM) + col);
;                 *(f32x4*)(xout + (size_t)row * DM + col) = r.x[bj][n] + gv * (acc[ai][bj][m][n] * isc); }
;     }
	v_pk_fma_f32 v[24:25], v[54:55], v[40:41], v[24:25]
	v_pk_fma_f32 v[22:23], v[56:57], v[38:39], v[22:23]
	v_pk_fma_f32 v[28:29], v[58:59], v[44:45], v[28:29]
	v_pk_fma_f32 v[26:27], v[60:61], v[42:43], v[26:27]
	v_pk_fma_f32 v[32:33], v[62:63], v[48:49], v[32:33]
	v_pk_fma_f32 v[30:31], v[64:65], v[46:47], v[30:31]
	v_pk_fma_f32 v[36:37], v[98:99], v[52:53], v[36:37]
	v_pk_fma_f32 v[34:35], v[100:101], v[50:51], v[34:35]
	global_store_dwordx4 v[102:103], v[22:25], off
	global_store_dwordx4 v[102:103], v[26:29], off offset:64
	global_store_dwordx4 v[102:103], v[30:33], off offset:512
	global_store_dwordx4 v[102:103], v[34:37], off offset:576
	global_load_dwordx4 v[22:25], v[106:107], off
	global_load_dwordx4 v[26:29], v[106:107], off offset:64
	global_load_dwordx4 v[30:33], v[106:107], off offset:512
	global_load_dwordx4 v[34:37], v[106:107], off offset:576
	v_pk_mul_f32 v[54:55], v[84:85], s[12:13] op_sel_hi:[1,0]
	v_pk_mul_f32 v[56:57], v[82:83], s[12:13] op_sel_hi:[1,0]
	v_pk_mul_f32 v[58:59], v[88:89], s[12:13] op_sel_hi:[1,0]
	v_pk_mul_f32 v[60:61], v[86:87], s[12:13] op_sel_hi:[1,0]
	v_pk_mul_f32 v[62:63], v[92:93], s[12:13] op_sel_hi:[1,0]
	v_pk_mul_f32 v[64:65], v[90:91], s[12:13] op_sel_hi:[1,0]
	v_pk_mul_f32 v[82:83], v[96:97], s[12:13] op_sel_hi:[1,0]
	v_pk_mul_f32 v[84:85], v[94:95], s[12:13] op_sel_hi:[1,0]
	v_lshl_add_u64 v[86:87], v[120:121], 0, v[2:3]
	s_waitcnt vmcnt(8)
	v_pk_fma_f32 v[20:21], v[54:55], v[40:41], v[20:21]
	v_pk_fma_f32 v[18:19], v[56:57], v[38:39], v[18:19]
	v_pk_fma_f32 v[16:17], v[58:59], v[44:45], v[16:17]
	v_pk_fma_f32 v[14:15], v[60:61], v[42:43], v[14:15]
	v_pk_fma_f32 v[12:13], v[62:63], v[48:49], v[12:13]
	v_pk_fma_f32 v[10:11], v[64:65], v[46:47], v[10:11]
	v_pk_fma_f32 v[8:9], v[82:83], v[52:53], v[8:9]
	v_pk_fma_f32 v[6:7], v[84:85], v[50:51], v[6:7]
	global_store_dwordx4 v[86:87], v[18:21], off
	global_store_dwordx4 v[86:87], v[14:17], off offset:64
	global_store_dwordx4 v[86:87], v[10:13], off offset:512
	global_store_dwordx4 v[86:87], v[6:9], off offset:576
	global_load_dwordx4 v[6:9], v[4:5], off
	global_load_dwordx4 v[10:13], v[4:5], off offset:64
	global_load_dwordx4 v[14:17], v[4:5], off offset:512
	global_load_dwordx4 v[18:21], v[4:5], off offset:576
	v_pk_mul_f32 v[4:5], v[68:69], s[12:13] op_sel_hi:[1,0]
	v_pk_mul_f32 v[38:39], v[66:67], s[12:13] op_sel_hi:[1,0]
	v_pk_mul_f32 v[40:41], v[72:73], s[12:13] op_sel_hi:[1,0]
	v_pk_mul_f32 v[42:43], v[70:71], s[12:13] op_sel_hi:[1,0]
	v_pk_mul_f32 v[44:45], v[76:77], s[12:13] op_sel_hi:[1,0]
	v_pk_mul_f32 v[46:47], v[74:75], s[12:13] op_sel_hi:[1,0]
	v_pk_mul_f32 v[48:49], v[80:81], s[12:13] op_sel_hi:[1,0]
	v_pk_mul_f32 v[50:51], v[78:79], s[12:13] op_sel_hi:[1,0]
	v_lshl_add_u64 v[52:53], v[104:105], 0, v[2:3]
	s_waitcnt vmcnt(0)
	v_pk_fma_f32 v[4:5], v[4:5], v[8:9], v[24:25]
	v_pk_fma_f32 v[2:3], v[38:39], v[6:7], v[22:23]
	v_pk_fma_f32 v[8:9], v[40:41], v[12:13], v[28:29]
	v_pk_fma_f32 v[6:7], v[42:43], v[10:11], v[26:27]
	v_pk_fma_f32 v[12:13], v[44:45], v[16:17], v[32:33]
	v_pk_fma_f32 v[10:11], v[46:47], v[14:15], v[30:31]
	v_pk_fma_f32 v[16:17], v[48:49], v[20:21], v[36:37]
	v_pk_fma_f32 v[14:15], v[50:51], v[18:19], v[34:35]
	global_store_dwordx4 v[52:53], v[2:5], off
	global_store_dwordx4 v[52:53], v[6:9], off offset:64
	global_store_dwordx4 v[52:53], v[10:13], off offset:512
	global_store_dwordx4 v[52:53], v[14:17], off offset:576
	s_cbranch_vccnz .LBB0_2515
	s_mov_b64 s[2:3], 0
	v_mov_b64 v[178:179], 0
	v_mov_b64 v[180:181], 0
	v_mov_b64 v[182:183], 0
	v_mov_b64 v[184:185], 0
	v_mov_b64 v[162:163], 0
	v_mov_b64 v[164:165], 0
	v_mov_b64 v[166:167], 0
	v_mov_b64 v[168:169], 0
	v_mov_b64 v[146:147], 0
	v_mov_b64 v[148:149], 0
	v_mov_b64 v[150:151], 0
	v_mov_b64 v[152:153], 0
	v_mov_b64 v[122:123], 0
	v_mov_b64 v[124:125], 0
	v_mov_b64 v[126:127], 0
	v_mov_b64 v[128:129], 0
	v_mov_b64 v[186:187], 0
	v_mov_b64 v[188:189], 0
	v_mov_b64 v[190:191], 0
	v_mov_b64 v[192:193], 0
	v_mov_b64 v[170:171], 0
	v_mov_b64 v[172:173], 0
	v_mov_b64 v[174:175], 0
	v_mov_b64 v[176:177], 0
	v_mov_b64 v[154:155], 0
	v_mov_b64 v[156:157], 0
	v_mov_b64 v[158:159], 0
	v_mov_b64 v[160:161], 0
	v_mov_b64 v[138:139], 0
	v_mov_b64 v[140:141], 0
	v_mov_b64 v[142:143], 0
	v_mov_b64 v[144:145], 0
	v_mov_b64 v[114:115], 0
	v_mov_b64 v[116:117], 0
	v_mov_b64 v[118:119], 0
	v_mov_b64 v[120:121], 0
	v_mov_b64 v[98:99], 0
	v_mov_b64 v[100:101], 0
	v_mov_b64 v[102:103], 0
	v_mov_b64 v[104:105], 0
	v_mov_b64 v[82:83], 0
	v_mov_b64 v[84:85], 0
	v_mov_b64 v[86:87], 0
	v_mov_b64 v[88:89], 0
	v_mov_b64 v[66:67], 0
	v_mov_b64 v[68:69], 0
	v_mov_b64 v[70:71], 0
	v_mov_b64 v[72:73], 0
	v_mov_b64 v[130:131], 0
	v_mov_b64 v[132:133], 0
	v_mov_b64 v[134:135], 0
	v_mov_b64 v[136:137], 0
	v_mov_b64 v[106:107], 0
	v_mov_b64 v[108:109], 0
	v_mov_b64 v[110:111], 0
	v_mov_b64 v[112:113], 0
	v_mov_b64 v[90:91], 0
	v_mov_b64 v[92:93], 0
	v_mov_b64 v[94:95], 0
	v_mov_b64 v[96:97], 0
	v_mov_b64 v[74:75], 0
	v_mov_b64 v[76:77], 0
	v_mov_b64 v[78:79], 0
	v_mov_b64 v[80:81], 0
	s_branch .LBB0_2515
